# GEMM phases (P1/P3/P5/P6): per-unit accumulator zeroing (128 v_mov per wave) removed; first K-loop trip peeled, each accumulator's first MFMA takes inline 0 as C
# speedup vs baseline: 1.0135x; 1.0135x over previous
.LBB0_125:
	s_mov_b32 s9, -2
	s_mov_b64 s[4:5], 0
	s_waitcnt vmcnt(8)
	.p2align 3
	s_nop 0
	ds_read_b128 v[130:133], v219
	ds_read_b128 v[134:137], v219 offset:2048
	ds_read_b128 v[138:141], v220
	ds_read_b128 v[142:145], v220 offset:2048
	ds_read_b128 v[146:149], v221
	ds_read_b128 v[150:153], v221 offset:2048
	ds_read_b128 v[154:157], v222
	ds_read_b128 v[158:161], v222 offset:2048
	ds_read_b128 v[162:165], v223
	ds_read_b128 v[166:169], v223 offset:2048
	ds_read_b128 v[170:173], v224
	ds_read_b128 v[174:177], v224 offset:2048
	ds_read_b128 v[178:181], v223 offset:4096
	ds_read_b128 v[182:185], v223 offset:6144
	ds_read_b128 v[186:189], v224 offset:4096
	ds_read_b128 v[190:193], v224 offset:6144
	s_add_u32 s47, s14, s4
	s_addc_u32 s50, s15, s5
	s_add_u32 s54, s47, 0x80
	s_addc_u32 s55, s50, 0
	s_mov_b32 m0, s70
	s_nop 0
	global_load_lds_dwordx4 v212, s[54:55] offset:0
	s_nop 0
	s_mov_b32 m0, s71
	s_nop 0
	global_load_lds_dwordx4 v214, s[54:55] offset:0
	s_waitcnt vmcnt(8)
	s_waitcnt lgkmcnt(0)
	s_barrier
	s_setprio 1
	s_waitcnt lgkmcnt(7)
	v_mfma_f32_16x16x32_bf16 v[126:129], v[130:133], v[162:165], 0
	v_mfma_f32_16x16x32_bf16 v[122:125], v[134:137], v[162:165], 0
	s_waitcnt lgkmcnt(6)
	v_mfma_f32_16x16x32_bf16 v[118:121], v[130:133], v[166:169], 0
	v_mfma_f32_16x16x32_bf16 v[114:117], v[134:137], v[166:169], 0
	s_waitcnt lgkmcnt(3)
	v_mfma_f32_16x16x32_bf16 v[110:113], v[130:133], v[178:181], 0
	v_mfma_f32_16x16x32_bf16 v[106:109], v[134:137], v[178:181], 0
	s_waitcnt lgkmcnt(2)
	v_mfma_f32_16x16x32_bf16 v[102:105], v[130:133], v[182:185], 0
	v_mfma_f32_16x16x32_bf16 v[98:101], v[134:137], v[182:185], 0
	v_mfma_f32_16x16x32_bf16 v[126:129], v[138:141], v[170:173], v[126:129]
	v_mfma_f32_16x16x32_bf16 v[122:125], v[142:145], v[170:173], v[122:125]
	v_mfma_f32_16x16x32_bf16 v[118:121], v[138:141], v[174:177], v[118:121]
	v_mfma_f32_16x16x32_bf16 v[114:117], v[142:145], v[174:177], v[114:117]
	s_waitcnt lgkmcnt(1)
	v_mfma_f32_16x16x32_bf16 v[110:113], v[138:141], v[186:189], v[110:113]
	v_mfma_f32_16x16x32_bf16 v[106:109], v[142:145], v[186:189], v[106:109]
	s_waitcnt lgkmcnt(0)
	v_mfma_f32_16x16x32_bf16 v[102:105], v[138:141], v[190:193], v[102:105]
	v_mfma_f32_16x16x32_bf16 v[98:101], v[142:145], v[190:193], v[98:101]
	s_setprio 0
	s_setprio 1
	v_mfma_f32_16x16x32_bf16 v[94:97], v[146:149], v[162:165], 0
	v_mfma_f32_16x16x32_bf16 v[90:93], v[150:153], v[162:165], 0
	v_mfma_f32_16x16x32_bf16 v[86:89], v[146:149], v[166:169], 0
	v_mfma_f32_16x16x32_bf16 v[82:85], v[150:153], v[166:169], 0
	v_mfma_f32_16x16x32_bf16 v[78:81], v[146:149], v[178:181], 0
	v_mfma_f32_16x16x32_bf16 v[74:77], v[150:153], v[178:181], 0
	v_mfma_f32_16x16x32_bf16 v[70:73], v[146:149], v[182:185], 0
	v_mfma_f32_16x16x32_bf16 v[66:69], v[150:153], v[182:185], 0
	v_mfma_f32_16x16x32_bf16 v[94:97], v[154:157], v[170:173], v[94:97]
	v_mfma_f32_16x16x32_bf16 v[90:93], v[158:161], v[170:173], v[90:93]
	v_mfma_f32_16x16x32_bf16 v[86:89], v[154:157], v[174:177], v[86:89]
	v_mfma_f32_16x16x32_bf16 v[82:85], v[158:161], v[174:177], v[82:85]
	v_mfma_f32_16x16x32_bf16 v[78:81], v[154:157], v[186:189], v[78:81]
	v_mfma_f32_16x16x32_bf16 v[74:77], v[158:161], v[186:189], v[74:77]
	v_mfma_f32_16x16x32_bf16 v[70:73], v[154:157], v[190:193], v[70:73]
	v_mfma_f32_16x16x32_bf16 v[66:69], v[158:161], v[190:193], v[66:69]
	s_setprio 0
	s_barrier
	s_add_u32 s51, s10, s4
	s_addc_u32 s53, s11, s5
	ds_read_b128 v[162:165], v223 offset:16384
	ds_read_b128 v[166:169], v223 offset:18432
	ds_read_b128 v[170:173], v224 offset:16384
	ds_read_b128 v[174:177], v224 offset:18432
	ds_read_b128 v[178:181], v223 offset:20480
	ds_read_b128 v[182:185], v223 offset:22528
	ds_read_b128 v[186:189], v224 offset:20480
	ds_read_b128 v[190:193], v224 offset:22528
	s_add_u32 s54, s51, 0x100
	s_addc_u32 s55, s53, 0
	s_mov_b32 m0, s57
	s_nop 0
	global_load_lds_dwordx4 v215, s[54:55] offset:0
	s_nop 0
	s_mov_b32 m0, s58
	s_nop 0
	global_load_lds_dwordx4 v216, s[54:55] offset:0
	s_add_u32 s54, s51, 0x40100
	s_addc_u32 s55, s53, 0
	s_mov_b32 m0, s59
	s_nop 0
	global_load_lds_dwordx4 v215, s[54:55] offset:0
	s_nop 0
	s_mov_b32 m0, s60
	s_nop 0
	global_load_lds_dwordx4 v216, s[54:55] offset:0
	s_add_u32 s54, s47, 0x100
	s_addc_u32 s55, s50, 0
	s_mov_b32 m0, s56
	s_nop 0
	global_load_lds_dwordx4 v211, s[54:55] offset:0
	s_nop 0
	s_mov_b32 m0, s61
	s_nop 0
	global_load_lds_dwordx4 v213, s[54:55] offset:0
	s_cmp_lg_u32 s9, 0xfffffffe
	s_cbranch_scc1 .Lrope_skip_ft
	s_lshl_b32 s100, s8, 14
	s_add_u32 s100, s96, s100
	s_addc_u32 s101, s97, 0
	s_mov_b32 m0, s98
	s_nop 0
	global_load_lds_dwordx4 v210, s[100:101] offset:0
	s_add_u32 s100, s100, 0x2000
	s_addc_u32 s101, s101, 0
	s_add_u32 s99, s98, 0x2000
	s_mov_b32 m0, s99
	s_nop 0
	global_load_lds_dwordx4 v210, s[100:101] offset:0
.Lrope_skip_ft:
	s_waitcnt vmcnt(8)
	s_waitcnt lgkmcnt(0)
	s_barrier
	s_setprio 1
	s_waitcnt lgkmcnt(7)
	v_mfma_f32_16x16x32_bf16 v[62:65], v[130:133], v[162:165], 0
	v_mfma_f32_16x16x32_bf16 v[58:61], v[134:137], v[162:165], 0
	s_waitcnt lgkmcnt(6)
	v_mfma_f32_16x16x32_bf16 v[54:57], v[130:133], v[166:169], 0
	v_mfma_f32_16x16x32_bf16 v[50:53], v[134:137], v[166:169], 0
	s_waitcnt lgkmcnt(3)
	v_mfma_f32_16x16x32_bf16 v[46:49], v[130:133], v[178:181], 0
	v_mfma_f32_16x16x32_bf16 v[42:45], v[134:137], v[178:181], 0
	s_waitcnt lgkmcnt(2)
	v_mfma_f32_16x16x32_bf16 v[38:41], v[130:133], v[182:185], 0
	v_mfma_f32_16x16x32_bf16 v[34:37], v[134:137], v[182:185], 0
	v_mfma_f32_16x16x32_bf16 v[62:65], v[138:141], v[170:173], v[62:65]
	v_mfma_f32_16x16x32_bf16 v[58:61], v[142:145], v[170:173], v[58:61]
	v_mfma_f32_16x16x32_bf16 v[54:57], v[138:141], v[174:177], v[54:57]
	v_mfma_f32_16x16x32_bf16 v[50:53], v[142:145], v[174:177], v[50:53]
	s_waitcnt lgkmcnt(1)
	v_mfma_f32_16x16x32_bf16 v[46:49], v[138:141], v[186:189], v[46:49]
	v_mfma_f32_16x16x32_bf16 v[42:45], v[142:145], v[186:189], v[42:45]
	s_waitcnt lgkmcnt(0)
	v_mfma_f32_16x16x32_bf16 v[38:41], v[138:141], v[190:193], v[38:41]
	v_mfma_f32_16x16x32_bf16 v[34:37], v[142:145], v[190:193], v[34:37]
	s_setprio 0
	s_setprio 1
	v_mfma_f32_16x16x32_bf16 v[30:33], v[146:149], v[162:165], 0
	v_mfma_f32_16x16x32_bf16 v[26:29], v[150:153], v[162:165], 0
	v_mfma_f32_16x16x32_bf16 v[22:25], v[146:149], v[166:169], 0
	v_mfma_f32_16x16x32_bf16 v[18:21], v[150:153], v[166:169], 0
	v_mfma_f32_16x16x32_bf16 v[14:17], v[146:149], v[178:181], 0
	v_mfma_f32_16x16x32_bf16 v[10:13], v[150:153], v[178:181], 0
	v_mfma_f32_16x16x32_bf16 v[6:9], v[146:149], v[182:185], 0
	v_mfma_f32_16x16x32_bf16 v[2:5], v[150:153], v[182:185], 0
	v_mfma_f32_16x16x32_bf16 v[30:33], v[154:157], v[170:173], v[30:33]
	v_mfma_f32_16x16x32_bf16 v[26:29], v[158:161], v[170:173], v[26:29]
	v_mfma_f32_16x16x32_bf16 v[22:25], v[154:157], v[174:177], v[22:25]
	v_mfma_f32_16x16x32_bf16 v[18:21], v[158:161], v[174:177], v[18:21]
	v_mfma_f32_16x16x32_bf16 v[14:17], v[154:157], v[186:189], v[14:17]
	v_mfma_f32_16x16x32_bf16 v[10:13], v[158:161], v[186:189], v[10:13]
	v_mfma_f32_16x16x32_bf16 v[6:9], v[154:157], v[190:193], v[6:9]
	v_mfma_f32_16x16x32_bf16 v[2:5], v[158:161], v[190:193], v[2:5]
	s_setprio 0
	s_barrier
	s_add_i32 s78, 0, 0x18000
	v_add_u32_e32 v162, s78, v217
	v_add_u32_e32 v163, s78, v218
	s_add_i32 s78, 0, 0x1c000
	v_add_u32_e32 v164, s78, v217
	ds_read_b128 v[130:133], v162
	ds_read_b128 v[134:137], v162 offset:2048
	ds_read_b128 v[138:141], v163
	ds_read_b128 v[142:145], v163 offset:2048
	v_add_u32_e32 v165, s78, v218
	ds_read_b128 v[146:149], v164
	ds_read_b128 v[150:153], v164 offset:2048
	ds_read_b128 v[154:157], v165
	ds_read_b128 v[158:161], v165 offset:2048
	ds_read_b128 v[166:169], v223 offset:32768
	ds_read_b128 v[170:173], v223 offset:34816
	ds_read_b128 v[174:177], v224 offset:32768
	ds_read_b128 v[178:181], v224 offset:34816
	ds_read_b128 v[182:185], v223 offset:36864
	ds_read_b128 v[186:189], v223 offset:38912
	ds_read_b128 v[190:193], v224 offset:36864
	ds_read_b128 v[198:201], v224 offset:38912
	s_mov_b32 m0, s62
	s_nop 0
	global_load_lds_dwordx4 v212, s[54:55] offset:0
	s_nop 0
	s_mov_b32 m0, s63
	s_nop 0
	global_load_lds_dwordx4 v214, s[54:55] offset:0
	s_waitcnt vmcnt(8)
	s_waitcnt lgkmcnt(0)
	s_barrier
	s_setprio 1
	s_waitcnt lgkmcnt(7)
	v_mfma_f32_16x16x32_bf16 v[126:129], v[130:133], v[166:169], v[126:129]
	v_mfma_f32_16x16x32_bf16 v[122:125], v[134:137], v[166:169], v[122:125]
	s_waitcnt lgkmcnt(6)
	v_mfma_f32_16x16x32_bf16 v[118:121], v[130:133], v[170:173], v[118:121]
	v_mfma_f32_16x16x32_bf16 v[114:117], v[134:137], v[170:173], v[114:117]
	s_waitcnt lgkmcnt(3)
	v_mfma_f32_16x16x32_bf16 v[110:113], v[130:133], v[182:185], v[110:113]
	v_mfma_f32_16x16x32_bf16 v[106:109], v[134:137], v[182:185], v[106:109]
	s_waitcnt lgkmcnt(2)
	v_mfma_f32_16x16x32_bf16 v[102:105], v[130:133], v[186:189], v[102:105]
	v_mfma_f32_16x16x32_bf16 v[98:101], v[134:137], v[186:189], v[98:101]
	v_mfma_f32_16x16x32_bf16 v[126:129], v[138:141], v[174:177], v[126:129]
	v_mfma_f32_16x16x32_bf16 v[122:125], v[142:145], v[174:177], v[122:125]
	v_mfma_f32_16x16x32_bf16 v[118:121], v[138:141], v[178:181], v[118:121]
	v_mfma_f32_16x16x32_bf16 v[114:117], v[142:145], v[178:181], v[114:117]
	s_waitcnt lgkmcnt(1)
	v_mfma_f32_16x16x32_bf16 v[110:113], v[138:141], v[190:193], v[110:113]
	v_mfma_f32_16x16x32_bf16 v[106:109], v[142:145], v[190:193], v[106:109]
	s_waitcnt lgkmcnt(0)
	v_mfma_f32_16x16x32_bf16 v[102:105], v[138:141], v[198:201], v[102:105]
	v_mfma_f32_16x16x32_bf16 v[98:101], v[142:145], v[198:201], v[98:101]
	s_setprio 0
	s_setprio 1
	v_mfma_f32_16x16x32_bf16 v[94:97], v[146:149], v[166:169], v[94:97]
	v_mfma_f32_16x16x32_bf16 v[90:93], v[150:153], v[166:169], v[90:93]
	v_mfma_f32_16x16x32_bf16 v[86:89], v[146:149], v[170:173], v[86:89]
	v_mfma_f32_16x16x32_bf16 v[82:85], v[150:153], v[170:173], v[82:85]
	v_mfma_f32_16x16x32_bf16 v[78:81], v[146:149], v[182:185], v[78:81]
	v_mfma_f32_16x16x32_bf16 v[74:77], v[150:153], v[182:185], v[74:77]
	v_mfma_f32_16x16x32_bf16 v[70:73], v[146:149], v[186:189], v[70:73]
	v_mfma_f32_16x16x32_bf16 v[66:69], v[150:153], v[186:189], v[66:69]
	v_mfma_f32_16x16x32_bf16 v[94:97], v[154:157], v[174:177], v[94:97]
	v_mfma_f32_16x16x32_bf16 v[90:93], v[158:161], v[174:177], v[90:93]
	v_mfma_f32_16x16x32_bf16 v[86:89], v[154:157], v[178:181], v[86:89]
	v_mfma_f32_16x16x32_bf16 v[82:85], v[158:161], v[178:181], v[82:85]
	v_mfma_f32_16x16x32_bf16 v[78:81], v[154:157], v[190:193], v[78:81]
	v_mfma_f32_16x16x32_bf16 v[74:77], v[158:161], v[190:193], v[74:77]
	v_mfma_f32_16x16x32_bf16 v[70:73], v[154:157], v[198:201], v[70:73]
	v_mfma_f32_16x16x32_bf16 v[66:69], v[158:161], v[198:201], v[66:69]
	s_setprio 0
	s_barrier
	ds_read_b128 v[166:169], v223 offset:49152
	ds_read_b128 v[170:173], v223 offset:51200
	ds_read_b128 v[174:177], v224 offset:49152
	ds_read_b128 v[178:181], v224 offset:51200
	ds_read_b128 v[182:185], v223 offset:53248
	ds_read_b128 v[186:189], v223 offset:55296
	ds_read_b128 v[190:193], v224 offset:53248
	ds_read_b128 v[198:201], v224 offset:55296
	s_add_u32 s54, s51, 0x180
	s_addc_u32 s55, s53, 0
	s_mov_b32 m0, s64
	s_nop 0
	global_load_lds_dwordx4 v215, s[54:55] offset:0
	s_nop 0
	s_mov_b32 m0, s65
	s_nop 0
	global_load_lds_dwordx4 v216, s[54:55] offset:0
	s_add_u32 s54, s51, 0x40180
	s_addc_u32 s55, s53, 0
	s_mov_b32 m0, s68
	s_nop 0
	global_load_lds_dwordx4 v215, s[54:55] offset:0
	s_nop 0
	s_mov_b32 m0, s69
	s_nop 0
	global_load_lds_dwordx4 v216, s[54:55] offset:0
	s_add_u32 s54, s47, 0x180
	s_addc_u32 s55, s50, 0
	s_mov_b32 m0, s66
	s_nop 0
	global_load_lds_dwordx4 v211, s[54:55] offset:0
	s_nop 0
	s_mov_b32 m0, s67
	s_nop 0
	global_load_lds_dwordx4 v213, s[54:55] offset:0
	s_waitcnt vmcnt(8)
	s_waitcnt lgkmcnt(0)
	s_barrier
	s_setprio 1
	s_waitcnt lgkmcnt(7)
	v_mfma_f32_16x16x32_bf16 v[62:65], v[130:133], v[166:169], v[62:65]
	v_mfma_f32_16x16x32_bf16 v[58:61], v[134:137], v[166:169], v[58:61]
	s_waitcnt lgkmcnt(6)
	v_mfma_f32_16x16x32_bf16 v[54:57], v[130:133], v[170:173], v[54:57]
	v_mfma_f32_16x16x32_bf16 v[50:53], v[134:137], v[170:173], v[50:53]
	s_waitcnt lgkmcnt(3)
	v_mfma_f32_16x16x32_bf16 v[46:49], v[130:133], v[182:185], v[46:49]
	v_mfma_f32_16x16x32_bf16 v[42:45], v[134:137], v[182:185], v[42:45]
	s_waitcnt lgkmcnt(2)
	v_mfma_f32_16x16x32_bf16 v[38:41], v[130:133], v[186:189], v[38:41]
	v_mfma_f32_16x16x32_bf16 v[34:37], v[134:137], v[186:189], v[34:37]
	v_mfma_f32_16x16x32_bf16 v[62:65], v[138:141], v[174:177], v[62:65]
	v_mfma_f32_16x16x32_bf16 v[58:61], v[142:145], v[174:177], v[58:61]
	v_mfma_f32_16x16x32_bf16 v[54:57], v[138:141], v[178:181], v[54:57]
	v_mfma_f32_16x16x32_bf16 v[50:53], v[142:145], v[178:181], v[50:53]
	s_waitcnt lgkmcnt(1)
	v_mfma_f32_16x16x32_bf16 v[46:49], v[138:141], v[190:193], v[46:49]
	v_mfma_f32_16x16x32_bf16 v[42:45], v[142:145], v[190:193], v[42:45]
	s_waitcnt lgkmcnt(0)
	v_mfma_f32_16x16x32_bf16 v[38:41], v[138:141], v[198:201], v[38:41]
	v_mfma_f32_16x16x32_bf16 v[34:37], v[142:145], v[198:201], v[34:37]
	s_setprio 0
	s_setprio 1
	v_mfma_f32_16x16x32_bf16 v[30:33], v[146:149], v[166:169], v[30:33]
	v_mfma_f32_16x16x32_bf16 v[26:29], v[150:153], v[166:169], v[26:29]
	v_mfma_f32_16x16x32_bf16 v[22:25], v[146:149], v[170:173], v[22:25]
	v_mfma_f32_16x16x32_bf16 v[18:21], v[150:153], v[170:173], v[18:21]
	v_mfma_f32_16x16x32_bf16 v[14:17], v[146:149], v[182:185], v[14:17]
	v_mfma_f32_16x16x32_bf16 v[10:13], v[150:153], v[182:185], v[10:13]
	v_mfma_f32_16x16x32_bf16 v[6:9], v[146:149], v[186:189], v[6:9]
	v_mfma_f32_16x16x32_bf16 v[2:5], v[150:153], v[186:189], v[2:5]
	v_mfma_f32_16x16x32_bf16 v[30:33], v[154:157], v[174:177], v[30:33]
	v_mfma_f32_16x16x32_bf16 v[26:29], v[158:161], v[174:177], v[26:29]
	v_mfma_f32_16x16x32_bf16 v[22:25], v[154:157], v[178:181], v[22:25]
	v_mfma_f32_16x16x32_bf16 v[18:21], v[158:161], v[178:181], v[18:21]
	v_mfma_f32_16x16x32_bf16 v[14:17], v[154:157], v[190:193], v[14:17]
	v_mfma_f32_16x16x32_bf16 v[10:13], v[158:161], v[190:193], v[10:13]
	v_mfma_f32_16x16x32_bf16 v[6:9], v[154:157], v[198:201], v[6:9]
	v_mfma_f32_16x16x32_bf16 v[2:5], v[158:161], v[198:201], v[2:5]
	s_setprio 0
	s_barrier
	s_add_i32 s9, s9, 2
	s_add_u32 s4, s4, 0x100
	s_addc_u32 s5, s5, 0

.LBB0_367:
	s_mov_b32 s31, -2
	s_mov_b64 s[6:7], 0
	.p2align 3
	s_nop 0
	ds_read_b128 v[130:133], v203
	ds_read_b128 v[134:137], v203 offset:2048
	ds_read_b128 v[138:141], v204
	ds_read_b128 v[142:145], v204 offset:2048
	ds_read_b128 v[146:149], v205
	ds_read_b128 v[150:153], v205 offset:2048
	ds_read_b128 v[154:157], v206
	ds_read_b128 v[158:161], v206 offset:2048
	ds_read_b128 v[162:165], v207
	ds_read_b128 v[166:169], v207 offset:2048
	ds_read_b128 v[174:177], v208
	ds_read_b128 v[178:181], v208 offset:2048
	ds_read_b128 v[182:185], v207 offset:4096
	ds_read_b128 v[210:213], v207 offset:6144
	ds_read_b128 v[214:217], v208 offset:4096
	ds_read_b128 v[218:221], v208 offset:6144
	s_add_u32 s36, s8, s6
	s_addc_u32 s37, s9, s7
	s_add_u32 s58, s36, 0x80
	s_addc_u32 s59, s37, 0
	s_mov_b32 m0, s52
	s_nop 0
	global_load_lds_dwordx4 v198, s[58:59] offset:0
	s_nop 0
	s_mov_b32 m0, s53
	s_nop 0
	global_load_lds_dwordx4 v200, s[58:59] offset:0
	s_waitcnt vmcnt(8)
	s_waitcnt lgkmcnt(0)
	s_barrier
	s_setprio 1
	s_waitcnt lgkmcnt(7)
	v_mfma_f32_16x16x32_bf16 v[126:129], v[130:133], v[162:165], 0
	v_mfma_f32_16x16x32_bf16 v[122:125], v[134:137], v[162:165], 0
	s_waitcnt lgkmcnt(6)
	v_mfma_f32_16x16x32_bf16 v[118:121], v[130:133], v[166:169], 0
	v_mfma_f32_16x16x32_bf16 v[114:117], v[134:137], v[166:169], 0
	s_waitcnt lgkmcnt(3)
	v_mfma_f32_16x16x32_bf16 v[110:113], v[130:133], v[182:185], 0
	v_mfma_f32_16x16x32_bf16 v[106:109], v[134:137], v[182:185], 0
	s_waitcnt lgkmcnt(2)
	v_mfma_f32_16x16x32_bf16 v[102:105], v[130:133], v[210:213], 0
	v_mfma_f32_16x16x32_bf16 v[98:101], v[134:137], v[210:213], 0
	v_mfma_f32_16x16x32_bf16 v[126:129], v[138:141], v[174:177], v[126:129]
	v_mfma_f32_16x16x32_bf16 v[122:125], v[142:145], v[174:177], v[122:125]
	v_mfma_f32_16x16x32_bf16 v[118:121], v[138:141], v[178:181], v[118:121]
	v_mfma_f32_16x16x32_bf16 v[114:117], v[142:145], v[178:181], v[114:117]
	s_waitcnt lgkmcnt(1)
	v_mfma_f32_16x16x32_bf16 v[110:113], v[138:141], v[214:217], v[110:113]
	v_mfma_f32_16x16x32_bf16 v[106:109], v[142:145], v[214:217], v[106:109]
	s_waitcnt lgkmcnt(0)
	v_mfma_f32_16x16x32_bf16 v[102:105], v[138:141], v[218:221], v[102:105]
	v_mfma_f32_16x16x32_bf16 v[98:101], v[142:145], v[218:221], v[98:101]
	s_setprio 0
	s_setprio 1
	v_mfma_f32_16x16x32_bf16 v[94:97], v[146:149], v[162:165], 0
	v_mfma_f32_16x16x32_bf16 v[90:93], v[150:153], v[162:165], 0
	v_mfma_f32_16x16x32_bf16 v[86:89], v[146:149], v[166:169], 0
	v_mfma_f32_16x16x32_bf16 v[82:85], v[150:153], v[166:169], 0
	v_mfma_f32_16x16x32_bf16 v[78:81], v[146:149], v[182:185], 0
	v_mfma_f32_16x16x32_bf16 v[74:77], v[150:153], v[182:185], 0
	v_mfma_f32_16x16x32_bf16 v[70:73], v[146:149], v[210:213], 0
	v_mfma_f32_16x16x32_bf16 v[66:69], v[150:153], v[210:213], 0
	v_mfma_f32_16x16x32_bf16 v[94:97], v[154:157], v[174:177], v[94:97]
	v_mfma_f32_16x16x32_bf16 v[90:93], v[158:161], v[174:177], v[90:93]
	v_mfma_f32_16x16x32_bf16 v[86:89], v[154:157], v[178:181], v[86:89]
	v_mfma_f32_16x16x32_bf16 v[82:85], v[158:161], v[178:181], v[82:85]
	v_mfma_f32_16x16x32_bf16 v[78:81], v[154:157], v[214:217], v[78:81]
	v_mfma_f32_16x16x32_bf16 v[74:77], v[158:161], v[214:217], v[74:77]
	v_mfma_f32_16x16x32_bf16 v[70:73], v[154:157], v[218:221], v[70:73]
	v_mfma_f32_16x16x32_bf16 v[66:69], v[158:161], v[218:221], v[66:69]
	s_setprio 0
	s_barrier
	s_add_u32 s60, s34, s6
	s_addc_u32 s61, s35, s7
	ds_read_b128 v[162:165], v207 offset:16384
	ds_read_b128 v[166:169], v207 offset:18432
	ds_read_b128 v[174:177], v208 offset:16384
	ds_read_b128 v[178:181], v208 offset:18432
	ds_read_b128 v[182:185], v207 offset:20480
	ds_read_b128 v[210:213], v207 offset:22528
	ds_read_b128 v[214:217], v208 offset:20480
	ds_read_b128 v[218:221], v208 offset:22528
	s_add_u32 s58, s60, 0x100
	s_addc_u32 s59, s61, 0
	s_mov_b32 m0, s39
	s_nop 0
	global_load_lds_dwordx4 v195, s[58:59] offset:0
	s_nop 0
	s_mov_b32 m0, s40
	s_nop 0
	global_load_lds_dwordx4 v196, s[58:59] offset:0
	s_add_u32 s58, s60, 0x40100
	s_addc_u32 s59, s61, 0
	s_mov_b32 m0, s41
	s_nop 0
	global_load_lds_dwordx4 v195, s[58:59] offset:0
	s_nop 0
	s_mov_b32 m0, s42
	s_nop 0
	global_load_lds_dwordx4 v196, s[58:59] offset:0
	s_add_u32 s58, s36, 0x100
	s_addc_u32 s59, s37, 0
	s_mov_b32 m0, s38
	s_nop 0
	global_load_lds_dwordx4 v197, s[58:59] offset:0
	s_nop 0
	s_mov_b32 m0, s43
	s_nop 0
	global_load_lds_dwordx4 v199, s[58:59] offset:0
	s_waitcnt vmcnt(8)
	s_waitcnt lgkmcnt(0)
	s_barrier
	s_setprio 1
	s_waitcnt lgkmcnt(7)
	v_mfma_f32_16x16x32_bf16 v[62:65], v[130:133], v[162:165], 0
	v_mfma_f32_16x16x32_bf16 v[58:61], v[134:137], v[162:165], 0
	s_waitcnt lgkmcnt(6)
	v_mfma_f32_16x16x32_bf16 v[54:57], v[130:133], v[166:169], 0
	v_mfma_f32_16x16x32_bf16 v[50:53], v[134:137], v[166:169], 0
	s_waitcnt lgkmcnt(3)
	v_mfma_f32_16x16x32_bf16 v[46:49], v[130:133], v[182:185], 0
	v_mfma_f32_16x16x32_bf16 v[42:45], v[134:137], v[182:185], 0
	s_waitcnt lgkmcnt(2)
	v_mfma_f32_16x16x32_bf16 v[38:41], v[130:133], v[210:213], 0
	v_mfma_f32_16x16x32_bf16 v[34:37], v[134:137], v[210:213], 0
	v_mfma_f32_16x16x32_bf16 v[62:65], v[138:141], v[174:177], v[62:65]
	v_mfma_f32_16x16x32_bf16 v[58:61], v[142:145], v[174:177], v[58:61]
	v_mfma_f32_16x16x32_bf16 v[54:57], v[138:141], v[178:181], v[54:57]
	v_mfma_f32_16x16x32_bf16 v[50:53], v[142:145], v[178:181], v[50:53]
	s_waitcnt lgkmcnt(1)
	v_mfma_f32_16x16x32_bf16 v[46:49], v[138:141], v[214:217], v[46:49]
	v_mfma_f32_16x16x32_bf16 v[42:45], v[142:145], v[214:217], v[42:45]
	s_waitcnt lgkmcnt(0)
	v_mfma_f32_16x16x32_bf16 v[38:41], v[138:141], v[218:221], v[38:41]
	v_mfma_f32_16x16x32_bf16 v[34:37], v[142:145], v[218:221], v[34:37]
	s_setprio 0
	s_setprio 1
	v_mfma_f32_16x16x32_bf16 v[30:33], v[146:149], v[162:165], 0
	v_mfma_f32_16x16x32_bf16 v[26:29], v[150:153], v[162:165], 0
	v_mfma_f32_16x16x32_bf16 v[22:25], v[146:149], v[166:169], 0
	v_mfma_f32_16x16x32_bf16 v[18:21], v[150:153], v[166:169], 0
	v_mfma_f32_16x16x32_bf16 v[14:17], v[146:149], v[182:185], 0
	v_mfma_f32_16x16x32_bf16 v[10:13], v[150:153], v[182:185], 0
	v_mfma_f32_16x16x32_bf16 v[6:9], v[146:149], v[210:213], 0
	v_mfma_f32_16x16x32_bf16 v[2:5], v[150:153], v[210:213], 0
	v_mfma_f32_16x16x32_bf16 v[30:33], v[154:157], v[174:177], v[30:33]
	v_mfma_f32_16x16x32_bf16 v[26:29], v[158:161], v[174:177], v[26:29]
	v_mfma_f32_16x16x32_bf16 v[22:25], v[154:157], v[178:181], v[22:25]
	v_mfma_f32_16x16x32_bf16 v[18:21], v[158:161], v[178:181], v[18:21]
	v_mfma_f32_16x16x32_bf16 v[14:17], v[154:157], v[214:217], v[14:17]
	v_mfma_f32_16x16x32_bf16 v[10:13], v[158:161], v[214:217], v[10:13]
	v_mfma_f32_16x16x32_bf16 v[6:9], v[154:157], v[218:221], v[6:9]
	v_mfma_f32_16x16x32_bf16 v[2:5], v[158:161], v[218:221], v[2:5]
	s_setprio 0
	s_barrier
	s_add_i32 s62, 0, 0x18000
	v_add_u32_e32 v174, s62, v201
	v_add_u32_e32 v175, s62, v202
	s_add_i32 s62, 0, 0x1c000
	v_add_u32_e32 v176, s62, v201
	ds_read_b128 v[130:133], v174
	ds_read_b128 v[134:137], v174 offset:2048
	ds_read_b128 v[138:141], v175
	ds_read_b128 v[142:145], v175 offset:2048
	v_add_u32_e32 v177, s62, v202
	ds_read_b128 v[146:149], v176
	ds_read_b128 v[150:153], v176 offset:2048
	ds_read_b128 v[154:157], v177
	ds_read_b128 v[158:161], v177 offset:2048
	ds_read_b128 v[162:165], v207 offset:32768
	ds_read_b128 v[166:169], v207 offset:34816
	ds_read_b128 v[178:181], v208 offset:32768
	ds_read_b128 v[182:185], v208 offset:34816
	ds_read_b128 v[210:213], v207 offset:36864
	ds_read_b128 v[214:217], v207 offset:38912
	ds_read_b128 v[218:221], v208 offset:36864
	ds_read_b128 v[222:225], v208 offset:38912
	s_mov_b32 m0, s44
	s_nop 0
	global_load_lds_dwordx4 v198, s[58:59] offset:0
	s_nop 0
	s_mov_b32 m0, s45
	s_nop 0
	global_load_lds_dwordx4 v200, s[58:59] offset:0
	s_waitcnt vmcnt(8)
	s_waitcnt lgkmcnt(0)
	s_barrier
	s_setprio 1
	s_waitcnt lgkmcnt(7)
	v_mfma_f32_16x16x32_bf16 v[126:129], v[130:133], v[162:165], v[126:129]
	v_mfma_f32_16x16x32_bf16 v[122:125], v[134:137], v[162:165], v[122:125]
	s_waitcnt lgkmcnt(6)
	v_mfma_f32_16x16x32_bf16 v[118:121], v[130:133], v[166:169], v[118:121]
	v_mfma_f32_16x16x32_bf16 v[114:117], v[134:137], v[166:169], v[114:117]
	s_waitcnt lgkmcnt(3)
	v_mfma_f32_16x16x32_bf16 v[110:113], v[130:133], v[210:213], v[110:113]
	v_mfma_f32_16x16x32_bf16 v[106:109], v[134:137], v[210:213], v[106:109]
	s_waitcnt lgkmcnt(2)
	v_mfma_f32_16x16x32_bf16 v[102:105], v[130:133], v[214:217], v[102:105]
	v_mfma_f32_16x16x32_bf16 v[98:101], v[134:137], v[214:217], v[98:101]
	v_mfma_f32_16x16x32_bf16 v[126:129], v[138:141], v[178:181], v[126:129]
	v_mfma_f32_16x16x32_bf16 v[122:125], v[142:145], v[178:181], v[122:125]
	v_mfma_f32_16x16x32_bf16 v[118:121], v[138:141], v[182:185], v[118:121]
	v_mfma_f32_16x16x32_bf16 v[114:117], v[142:145], v[182:185], v[114:117]
	s_waitcnt lgkmcnt(1)
	v_mfma_f32_16x16x32_bf16 v[110:113], v[138:141], v[218:221], v[110:113]
	v_mfma_f32_16x16x32_bf16 v[106:109], v[142:145], v[218:221], v[106:109]
	s_waitcnt lgkmcnt(0)
	v_mfma_f32_16x16x32_bf16 v[102:105], v[138:141], v[222:225], v[102:105]
	v_mfma_f32_16x16x32_bf16 v[98:101], v[142:145], v[222:225], v[98:101]
	s_setprio 0
	s_setprio 1
	v_mfma_f32_16x16x32_bf16 v[94:97], v[146:149], v[162:165], v[94:97]
	v_mfma_f32_16x16x32_bf16 v[90:93], v[150:153], v[162:165], v[90:93]
	v_mfma_f32_16x16x32_bf16 v[86:89], v[146:149], v[166:169], v[86:89]
	v_mfma_f32_16x16x32_bf16 v[82:85], v[150:153], v[166:169], v[82:85]
	v_mfma_f32_16x16x32_bf16 v[78:81], v[146:149], v[210:213], v[78:81]
	v_mfma_f32_16x16x32_bf16 v[74:77], v[150:153], v[210:213], v[74:77]
	v_mfma_f32_16x16x32_bf16 v[70:73], v[146:149], v[214:217], v[70:73]
	v_mfma_f32_16x16x32_bf16 v[66:69], v[150:153], v[214:217], v[66:69]
	v_mfma_f32_16x16x32_bf16 v[94:97], v[154:157], v[178:181], v[94:97]
	v_mfma_f32_16x16x32_bf16 v[90:93], v[158:161], v[178:181], v[90:93]
	v_mfma_f32_16x16x32_bf16 v[86:89], v[154:157], v[182:185], v[86:89]
	v_mfma_f32_16x16x32_bf16 v[82:85], v[158:161], v[182:185], v[82:85]
	v_mfma_f32_16x16x32_bf16 v[78:81], v[154:157], v[218:221], v[78:81]
	v_mfma_f32_16x16x32_bf16 v[74:77], v[158:161], v[218:221], v[74:77]
	v_mfma_f32_16x16x32_bf16 v[70:73], v[154:157], v[222:225], v[70:73]
	v_mfma_f32_16x16x32_bf16 v[66:69], v[158:161], v[222:225], v[66:69]
	s_setprio 0
	s_barrier
	ds_read_b128 v[162:165], v207 offset:49152
	ds_read_b128 v[166:169], v207 offset:51200
	ds_read_b128 v[178:181], v208 offset:49152
	ds_read_b128 v[182:185], v208 offset:51200
	ds_read_b128 v[210:213], v207 offset:53248
	ds_read_b128 v[214:217], v207 offset:55296
	ds_read_b128 v[218:221], v208 offset:53248
	ds_read_b128 v[222:225], v208 offset:55296
	s_add_u32 s58, s60, 0x180
	s_addc_u32 s59, s61, 0
	s_mov_b32 m0, s46
	s_nop 0
	global_load_lds_dwordx4 v195, s[58:59] offset:0
	s_nop 0
	s_mov_b32 m0, s47
	s_nop 0
	global_load_lds_dwordx4 v196, s[58:59] offset:0
	s_add_u32 s58, s60, 0x40180
	s_addc_u32 s59, s61, 0
	s_mov_b32 m0, s50
	s_nop 0
	global_load_lds_dwordx4 v195, s[58:59] offset:0
	s_add_u32 s36, s36, 0x180
	s_mov_b32 m0, s51
	s_nop 0
	global_load_lds_dwordx4 v196, s[58:59] offset:0
	s_addc_u32 s37, s37, 0
	s_mov_b32 m0, s48
	s_nop 0
	global_load_lds_dwordx4 v197, s[36:37] offset:0
	s_nop 0
	s_mov_b32 m0, s49
	s_nop 0
	global_load_lds_dwordx4 v199, s[36:37] offset:0
	s_waitcnt vmcnt(8)
	s_waitcnt lgkmcnt(0)
	s_barrier
	s_setprio 1
	s_waitcnt lgkmcnt(7)
	v_mfma_f32_16x16x32_bf16 v[62:65], v[130:133], v[162:165], v[62:65]
	v_mfma_f32_16x16x32_bf16 v[58:61], v[134:137], v[162:165], v[58:61]
	s_waitcnt lgkmcnt(6)
	v_mfma_f32_16x16x32_bf16 v[54:57], v[130:133], v[166:169], v[54:57]
	v_mfma_f32_16x16x32_bf16 v[50:53], v[134:137], v[166:169], v[50:53]
	s_waitcnt lgkmcnt(3)
	v_mfma_f32_16x16x32_bf16 v[46:49], v[130:133], v[210:213], v[46:49]
	v_mfma_f32_16x16x32_bf16 v[42:45], v[134:137], v[210:213], v[42:45]
	s_waitcnt lgkmcnt(2)
	v_mfma_f32_16x16x32_bf16 v[38:41], v[130:133], v[214:217], v[38:41]
	v_mfma_f32_16x16x32_bf16 v[34:37], v[134:137], v[214:217], v[34:37]
	v_mfma_f32_16x16x32_bf16 v[62:65], v[138:141], v[178:181], v[62:65]
	v_mfma_f32_16x16x32_bf16 v[58:61], v[142:145], v[178:181], v[58:61]
	v_mfma_f32_16x16x32_bf16 v[54:57], v[138:141], v[182:185], v[54:57]
	v_mfma_f32_16x16x32_bf16 v[50:53], v[142:145], v[182:185], v[50:53]
	s_waitcnt lgkmcnt(1)
	v_mfma_f32_16x16x32_bf16 v[46:49], v[138:141], v[218:221], v[46:49]
	v_mfma_f32_16x16x32_bf16 v[42:45], v[142:145], v[218:221], v[42:45]
	s_waitcnt lgkmcnt(0)
	v_mfma_f32_16x16x32_bf16 v[38:41], v[138:141], v[222:225], v[38:41]
	v_mfma_f32_16x16x32_bf16 v[34:37], v[142:145], v[222:225], v[34:37]
	s_setprio 0
	s_setprio 1
	v_mfma_f32_16x16x32_bf16 v[30:33], v[146:149], v[162:165], v[30:33]
	v_mfma_f32_16x16x32_bf16 v[26:29], v[150:153], v[162:165], v[26:29]
	v_mfma_f32_16x16x32_bf16 v[22:25], v[146:149], v[166:169], v[22:25]
	v_mfma_f32_16x16x32_bf16 v[18:21], v[150:153], v[166:169], v[18:21]
	v_mfma_f32_16x16x32_bf16 v[14:17], v[146:149], v[210:213], v[14:17]
	v_mfma_f32_16x16x32_bf16 v[10:13], v[150:153], v[210:213], v[10:13]
	v_mfma_f32_16x16x32_bf16 v[6:9], v[146:149], v[214:217], v[6:9]
	v_mfma_f32_16x16x32_bf16 v[2:5], v[150:153], v[214:217], v[2:5]
	v_mfma_f32_16x16x32_bf16 v[30:33], v[154:157], v[178:181], v[30:33]
	v_mfma_f32_16x16x32_bf16 v[26:29], v[158:161], v[178:181], v[26:29]
	v_mfma_f32_16x16x32_bf16 v[22:25], v[154:157], v[182:185], v[22:25]
	v_mfma_f32_16x16x32_bf16 v[18:21], v[158:161], v[182:185], v[18:21]
	v_mfma_f32_16x16x32_bf16 v[14:17], v[154:157], v[218:221], v[14:17]
	v_mfma_f32_16x16x32_bf16 v[10:13], v[158:161], v[218:221], v[10:13]
	v_mfma_f32_16x16x32_bf16 v[6:9], v[154:157], v[222:225], v[6:9]
	v_mfma_f32_16x16x32_bf16 v[2:5], v[158:161], v[222:225], v[2:5]
	s_setprio 0
	s_barrier
	s_add_i32 s31, s31, 2
	s_add_u32 s6, s6, 0x100
	s_addc_u32 s7, s7, 0

.LBB0_560:
	s_mov_b32 s35, -2
	.p2align 3
	s_nop 0
	ds_read_b128 v[18:21], v179
	ds_read_b128 v[26:29], v179 offset:2048
	ds_read_b128 v[22:25], v180
	ds_read_b128 v[30:33], v180 offset:2048
	ds_read_b128 v[2:5], v181
	ds_read_b128 v[10:13], v181 offset:2048
	ds_read_b128 v[6:9], v182
	ds_read_b128 v[14:17], v182 offset:2048
	ds_read_b128 v[194:197], v183
	ds_read_b128 v[202:205], v183 offset:2048
	ds_read_b128 v[198:201], v184
	ds_read_b128 v[206:209], v184 offset:2048
	ds_read_b128 v[210:213], v183 offset:4096
	ds_read_b128 v[218:221], v183 offset:6144
	ds_read_b128 v[214:217], v184 offset:4096
	ds_read_b128 v[222:225], v184 offset:6144
	s_add_u32 s39, s18, s4
	s_addc_u32 s68, s19, s5
	s_add_u32 s42, s39, 0x80
	s_addc_u32 s43, s68, 0
	s_mov_b32 m0, s61
	s_nop 0
	global_load_lds_dwordx4 v172, s[42:43] offset:0
	s_nop 0
	s_mov_b32 m0, s62
	s_nop 0
	global_load_lds_dwordx4 v175, s[42:43] offset:0
	s_waitcnt vmcnt(8)
	s_waitcnt lgkmcnt(0)
	s_barrier
	s_setprio 1
	s_waitcnt lgkmcnt(5)
	v_mfma_f32_16x16x128_f8f6f4 v[158:161], v[18:25], v[194:201], 0
	v_mfma_f32_16x16x128_f8f6f4 v[150:153], v[26:33], v[194:201], 0
	s_waitcnt lgkmcnt(4)
	v_mfma_f32_16x16x128_f8f6f4 v[142:145], v[18:25], v[202:209], 0
	v_mfma_f32_16x16x128_f8f6f4 v[134:137], v[26:33], v[202:209], 0
	s_waitcnt lgkmcnt(1)
	v_mfma_f32_16x16x128_f8f6f4 v[126:129], v[18:25], v[210:217], 0
	v_mfma_f32_16x16x128_f8f6f4 v[118:121], v[26:33], v[210:217], 0
	s_waitcnt lgkmcnt(0)
	v_mfma_f32_16x16x128_f8f6f4 v[110:113], v[18:25], v[218:225], 0
	v_mfma_f32_16x16x128_f8f6f4 v[102:105], v[26:33], v[218:225], 0
	s_setprio 0
	s_setprio 1
	v_mfma_f32_16x16x128_f8f6f4 v[154:157], v[2:9], v[194:201], 0
	v_mfma_f32_16x16x128_f8f6f4 v[146:149], v[10:17], v[194:201], 0
	v_mfma_f32_16x16x128_f8f6f4 v[138:141], v[2:9], v[202:209], 0
	v_mfma_f32_16x16x128_f8f6f4 v[130:133], v[10:17], v[202:209], 0
	v_mfma_f32_16x16x128_f8f6f4 v[122:125], v[2:9], v[210:217], 0
	v_mfma_f32_16x16x128_f8f6f4 v[114:117], v[10:17], v[210:217], 0
	v_mfma_f32_16x16x128_f8f6f4 v[106:109], v[2:9], v[218:225], 0
	v_mfma_f32_16x16x128_f8f6f4 v[98:101], v[10:17], v[218:225], 0
	s_setprio 0
	s_barrier
	s_add_u32 s69, s44, s4
	s_addc_u32 s70, s45, s5
	ds_read_b128 v[194:197], v183 offset:16384
	ds_read_b128 v[202:205], v183 offset:18432
	ds_read_b128 v[198:201], v184 offset:16384
	ds_read_b128 v[206:209], v184 offset:18432
	ds_read_b128 v[210:213], v183 offset:20480
	ds_read_b128 v[218:221], v183 offset:22528
	ds_read_b128 v[214:217], v184 offset:20480
	ds_read_b128 v[222:225], v184 offset:22528
	s_add_u32 s42, s69, 0x100
	s_addc_u32 s43, s70, 0
	s_mov_b32 m0, s48
	s_nop 0
	global_load_lds_dwordx4 v1, s[42:43] offset:0
	s_nop 0
	s_mov_b32 m0, s49
	s_nop 0
	global_load_lds_dwordx4 v173, s[42:43] offset:0
	s_add_u32 s42, s69, 0x20100
	s_addc_u32 s43, s70, 0
	s_mov_b32 m0, s50
	s_nop 0
	global_load_lds_dwordx4 v1, s[42:43] offset:0
	s_nop 0
	s_mov_b32 m0, s51
	s_nop 0
	global_load_lds_dwordx4 v173, s[42:43] offset:0
	s_add_u32 s42, s39, 0x100
	s_addc_u32 s43, s68, 0
	s_mov_b32 m0, s29
	s_nop 0
	global_load_lds_dwordx4 v171, s[42:43] offset:0
	s_nop 0
	s_mov_b32 m0, s52
	s_nop 0
	global_load_lds_dwordx4 v174, s[42:43] offset:0
	s_waitcnt vmcnt(8)
	s_waitcnt lgkmcnt(0)
	s_barrier
	s_setprio 1
	s_waitcnt lgkmcnt(5)
	v_mfma_f32_16x16x128_f8f6f4 v[94:97], v[18:25], v[194:201], 0
	v_mfma_f32_16x16x128_f8f6f4 v[86:89], v[26:33], v[194:201], 0
	s_waitcnt lgkmcnt(4)
	v_mfma_f32_16x16x128_f8f6f4 v[78:81], v[18:25], v[202:209], 0
	v_mfma_f32_16x16x128_f8f6f4 v[70:73], v[26:33], v[202:209], 0
	s_waitcnt lgkmcnt(1)
	v_mfma_f32_16x16x128_f8f6f4 v[62:65], v[18:25], v[210:217], 0
	v_mfma_f32_16x16x128_f8f6f4 v[54:57], v[26:33], v[210:217], 0
	s_waitcnt lgkmcnt(0)
	v_mfma_f32_16x16x128_f8f6f4 v[46:49], v[18:25], v[218:225], 0
	v_mfma_f32_16x16x128_f8f6f4 v[38:41], v[26:33], v[218:225], 0
	s_setprio 0
	s_setprio 1
	v_mfma_f32_16x16x128_f8f6f4 v[90:93], v[2:9], v[194:201], 0
	v_mfma_f32_16x16x128_f8f6f4 v[82:85], v[10:17], v[194:201], 0
	v_mfma_f32_16x16x128_f8f6f4 v[74:77], v[2:9], v[202:209], 0
	v_mfma_f32_16x16x128_f8f6f4 v[66:69], v[10:17], v[202:209], 0
	v_mfma_f32_16x16x128_f8f6f4 v[58:61], v[2:9], v[210:217], 0
	v_mfma_f32_16x16x128_f8f6f4 v[50:53], v[10:17], v[210:217], 0
	v_mfma_f32_16x16x128_f8f6f4 v[42:45], v[2:9], v[218:225], 0
	v_mfma_f32_16x16x128_f8f6f4 v[34:37], v[10:17], v[218:225], 0
	s_setprio 0
	s_barrier
	s_add_i32 s71, 0, 0x18000
	v_add_u32_e32 v162, s71, v176
	v_add_u32_e32 v187, s71, v177
	s_add_i32 s71, 0, 0x1c000
	v_add_u32_e32 v194, s71, v176
	ds_read_b128 v[2:5], v162
	ds_read_b128 v[10:13], v162 offset:2048
	ds_read_b128 v[6:9], v187
	ds_read_b128 v[14:17], v187 offset:2048
	v_add_u32_e32 v195, s71, v177
	ds_read_b128 v[18:21], v194
	ds_read_b128 v[26:29], v194 offset:2048
	ds_read_b128 v[22:25], v195
	ds_read_b128 v[30:33], v195 offset:2048
	ds_read_b128 v[196:199], v183 offset:32768
	ds_read_b128 v[204:207], v183 offset:34816
	ds_read_b128 v[200:203], v184 offset:32768
	ds_read_b128 v[208:211], v184 offset:34816
	ds_read_b128 v[212:215], v183 offset:36864
	ds_read_b128 v[220:223], v183 offset:38912
	ds_read_b128 v[216:219], v184 offset:36864
	ds_read_b128 v[224:227], v184 offset:38912
	s_mov_b32 m0, s53
	s_nop 0
	global_load_lds_dwordx4 v172, s[42:43] offset:0
	s_nop 0
	s_mov_b32 m0, s54
	s_nop 0
	global_load_lds_dwordx4 v175, s[42:43] offset:0
	s_waitcnt vmcnt(8)
	s_waitcnt lgkmcnt(0)
	s_barrier
	s_setprio 1
	s_waitcnt lgkmcnt(5)
	v_mfma_f32_16x16x128_f8f6f4 v[158:161], v[2:9], v[196:203], v[158:161]
	v_mfma_f32_16x16x128_f8f6f4 v[150:153], v[10:17], v[196:203], v[150:153]
	s_waitcnt lgkmcnt(4)
	v_mfma_f32_16x16x128_f8f6f4 v[142:145], v[2:9], v[204:211], v[142:145]
	v_mfma_f32_16x16x128_f8f6f4 v[134:137], v[10:17], v[204:211], v[134:137]
	s_waitcnt lgkmcnt(1)
	v_mfma_f32_16x16x128_f8f6f4 v[126:129], v[2:9], v[212:219], v[126:129]
	v_mfma_f32_16x16x128_f8f6f4 v[118:121], v[10:17], v[212:219], v[118:121]
	s_waitcnt lgkmcnt(0)
	v_mfma_f32_16x16x128_f8f6f4 v[110:113], v[2:9], v[220:227], v[110:113]
	v_mfma_f32_16x16x128_f8f6f4 v[102:105], v[10:17], v[220:227], v[102:105]
	s_setprio 0
	s_setprio 1
	v_mfma_f32_16x16x128_f8f6f4 v[154:157], v[18:25], v[196:203], v[154:157]
	v_mfma_f32_16x16x128_f8f6f4 v[146:149], v[26:33], v[196:203], v[146:149]
	v_mfma_f32_16x16x128_f8f6f4 v[138:141], v[18:25], v[204:211], v[138:141]
	v_mfma_f32_16x16x128_f8f6f4 v[130:133], v[26:33], v[204:211], v[130:133]
	v_mfma_f32_16x16x128_f8f6f4 v[122:125], v[18:25], v[212:219], v[122:125]
	v_mfma_f32_16x16x128_f8f6f4 v[114:117], v[26:33], v[212:219], v[114:117]
	v_mfma_f32_16x16x128_f8f6f4 v[106:109], v[18:25], v[220:227], v[106:109]
	v_mfma_f32_16x16x128_f8f6f4 v[98:101], v[26:33], v[220:227], v[98:101]
	s_setprio 0
	s_barrier
	ds_read_b128 v[196:199], v183 offset:49152
	ds_read_b128 v[204:207], v183 offset:51200
	ds_read_b128 v[200:203], v184 offset:49152
	ds_read_b128 v[208:211], v184 offset:51200
	ds_read_b128 v[212:215], v183 offset:53248
	ds_read_b128 v[220:223], v183 offset:55296
	ds_read_b128 v[216:219], v184 offset:53248
	ds_read_b128 v[224:227], v184 offset:55296
	s_add_u32 s42, s69, 0x180
	s_addc_u32 s43, s70, 0
	s_mov_b32 m0, s55
	s_nop 0
	global_load_lds_dwordx4 v1, s[42:43] offset:0
	s_nop 0
	s_mov_b32 m0, s56
	s_nop 0
	global_load_lds_dwordx4 v173, s[42:43] offset:0
	s_add_u32 s42, s69, 0x20180
	s_addc_u32 s43, s70, 0
	s_mov_b32 m0, s59
	s_nop 0
	global_load_lds_dwordx4 v1, s[42:43] offset:0
	s_nop 0
	s_mov_b32 m0, s60
	s_nop 0
	global_load_lds_dwordx4 v173, s[42:43] offset:0
	s_add_u32 s42, s39, 0x180
	s_addc_u32 s43, s68, 0
	s_mov_b32 m0, s57
	s_nop 0
	global_load_lds_dwordx4 v171, s[42:43] offset:0
	s_nop 0
	s_mov_b32 m0, s58
	s_nop 0
	global_load_lds_dwordx4 v174, s[42:43] offset:0
	s_waitcnt vmcnt(8)
	s_waitcnt lgkmcnt(0)
	s_barrier
	s_setprio 1
	s_waitcnt lgkmcnt(5)
	v_mfma_f32_16x16x128_f8f6f4 v[94:97], v[2:9], v[196:203], v[94:97]
	v_mfma_f32_16x16x128_f8f6f4 v[86:89], v[10:17], v[196:203], v[86:89]
	s_waitcnt lgkmcnt(4)
	v_mfma_f32_16x16x128_f8f6f4 v[78:81], v[2:9], v[204:211], v[78:81]
	v_mfma_f32_16x16x128_f8f6f4 v[70:73], v[10:17], v[204:211], v[70:73]
	s_waitcnt lgkmcnt(1)
	v_mfma_f32_16x16x128_f8f6f4 v[62:65], v[2:9], v[212:219], v[62:65]
	v_mfma_f32_16x16x128_f8f6f4 v[54:57], v[10:17], v[212:219], v[54:57]
	s_waitcnt lgkmcnt(0)
	v_mfma_f32_16x16x128_f8f6f4 v[46:49], v[2:9], v[220:227], v[46:49]
	v_mfma_f32_16x16x128_f8f6f4 v[38:41], v[10:17], v[220:227], v[38:41]
	s_setprio 0
	s_setprio 1
	v_mfma_f32_16x16x128_f8f6f4 v[90:93], v[18:25], v[196:203], v[90:93]
	v_mfma_f32_16x16x128_f8f6f4 v[82:85], v[26:33], v[196:203], v[82:85]
	v_mfma_f32_16x16x128_f8f6f4 v[74:77], v[18:25], v[204:211], v[74:77]
	v_mfma_f32_16x16x128_f8f6f4 v[66:69], v[26:33], v[204:211], v[66:69]
	v_mfma_f32_16x16x128_f8f6f4 v[58:61], v[18:25], v[212:219], v[58:61]
	v_mfma_f32_16x16x128_f8f6f4 v[50:53], v[26:33], v[212:219], v[50:53]
	v_mfma_f32_16x16x128_f8f6f4 v[42:45], v[18:25], v[220:227], v[42:45]
	v_mfma_f32_16x16x128_f8f6f4 v[34:37], v[26:33], v[220:227], v[34:37]
	s_setprio 0
	s_barrier
	s_add_i32 s35, s35, 2
	s_add_u32 s4, s4, 0x100
	s_addc_u32 s5, s5, 0

.LBB0_649:
	s_mov_b32 s35, -2
	.p2align 3
	s_nop 0
	ds_read_b128 v[18:21], v176
	ds_read_b128 v[26:29], v176 offset:2048
	ds_read_b128 v[22:25], v177
	ds_read_b128 v[30:33], v177 offset:2048
	ds_read_b128 v[2:5], v178
	ds_read_b128 v[10:13], v178 offset:2048
	ds_read_b128 v[6:9], v179
	ds_read_b128 v[14:17], v179 offset:2048
	ds_read_b128 v[194:197], v180
	ds_read_b128 v[202:205], v180 offset:2048
	ds_read_b128 v[198:201], v181
	ds_read_b128 v[206:209], v181 offset:2048
	ds_read_b128 v[210:213], v180 offset:4096
	ds_read_b128 v[218:221], v180 offset:6144
	ds_read_b128 v[214:217], v181 offset:4096
	ds_read_b128 v[222:225], v181 offset:6144
	s_add_u32 s64, s12, s4
	s_addc_u32 s65, s13, s5
	s_add_u32 s46, s64, 0x80
	s_addc_u32 s47, s65, 0
	s_mov_b32 m0, s58
	s_nop 0
	global_load_lds_dwordx4 v163, s[46:47] offset:0
	s_nop 0
	s_mov_b32 m0, s59
	s_nop 0
	global_load_lds_dwordx4 v171, s[46:47] offset:0
	s_waitcnt vmcnt(8)
	s_waitcnt lgkmcnt(0)
	s_barrier
	s_setprio 1
	s_waitcnt lgkmcnt(0)
	v_mfma_f32_16x16x128_f8f6f4 v[158:161], v[18:25], v[194:201], 0
	v_mfma_f32_16x16x128_f8f6f4 v[154:157], v[26:33], v[194:201], 0
	v_mfma_f32_16x16x128_f8f6f4 v[142:145], v[18:25], v[202:209], 0
	v_mfma_f32_16x16x128_f8f6f4 v[138:141], v[26:33], v[202:209], 0
	v_mfma_f32_16x16x128_f8f6f4 v[126:129], v[18:25], v[210:217], 0
	v_mfma_f32_16x16x128_f8f6f4 v[122:125], v[26:33], v[210:217], 0
	v_mfma_f32_16x16x128_f8f6f4 v[110:113], v[18:25], v[218:225], 0
	v_mfma_f32_16x16x128_f8f6f4 v[106:109], v[26:33], v[218:225], 0
	s_setprio 0
	s_setprio 1
	v_mfma_f32_16x16x128_f8f6f4 v[150:153], v[2:9], v[194:201], 0
	v_mfma_f32_16x16x128_f8f6f4 v[146:149], v[10:17], v[194:201], 0
	v_mfma_f32_16x16x128_f8f6f4 v[134:137], v[2:9], v[202:209], 0
	v_mfma_f32_16x16x128_f8f6f4 v[130:133], v[10:17], v[202:209], 0
	v_mfma_f32_16x16x128_f8f6f4 v[118:121], v[2:9], v[210:217], 0
	v_mfma_f32_16x16x128_f8f6f4 v[114:117], v[10:17], v[210:217], 0
	v_mfma_f32_16x16x128_f8f6f4 v[102:105], v[2:9], v[218:225], 0
	v_mfma_f32_16x16x128_f8f6f4 v[98:101], v[10:17], v[218:225], 0
	s_setprio 0
	s_barrier
	s_add_u32 s66, s42, s4
	s_addc_u32 s67, s43, s5
	ds_read_b128 v[194:197], v180 offset:16384
	ds_read_b128 v[202:205], v180 offset:18432
	ds_read_b128 v[198:201], v181 offset:16384
	ds_read_b128 v[206:209], v181 offset:18432
	ds_read_b128 v[210:213], v180 offset:20480
	ds_read_b128 v[218:221], v180 offset:22528
	ds_read_b128 v[214:217], v181 offset:20480
	ds_read_b128 v[222:225], v181 offset:22528
	s_add_u32 s46, s66, 0x100
	s_addc_u32 s47, s67, 0
	s_mov_b32 m0, s33
	s_nop 0
	global_load_lds_dwordx4 v172, s[46:47] offset:0
	s_nop 0
	s_mov_b32 m0, s39
	s_nop 0
	global_load_lds_dwordx4 v173, s[46:47] offset:0
	s_add_u32 s46, s66, 0x20100
	s_addc_u32 s47, s67, 0
	s_mov_b32 m0, s41
	s_nop 0
	global_load_lds_dwordx4 v172, s[46:47] offset:0
	s_nop 0
	s_mov_b32 m0, s48
	s_nop 0
	global_load_lds_dwordx4 v173, s[46:47] offset:0
	s_add_u32 s46, s64, 0x100
	s_addc_u32 s47, s65, 0
	s_mov_b32 m0, s1
	s_nop 0
	global_load_lds_dwordx4 v162, s[46:47] offset:0
	s_nop 0
	s_mov_b32 m0, s49
	s_nop 0
	global_load_lds_dwordx4 v170, s[46:47] offset:0
	s_waitcnt vmcnt(8)
	s_waitcnt lgkmcnt(0)
	s_barrier
	s_setprio 1
	s_waitcnt lgkmcnt(5)
	v_mfma_f32_16x16x128_f8f6f4 v[94:97], v[18:25], v[194:201], 0
	v_mfma_f32_16x16x128_f8f6f4 v[90:93], v[26:33], v[194:201], 0
	s_waitcnt lgkmcnt(4)
	v_mfma_f32_16x16x128_f8f6f4 v[78:81], v[18:25], v[202:209], 0
	v_mfma_f32_16x16x128_f8f6f4 v[74:77], v[26:33], v[202:209], 0
	s_waitcnt lgkmcnt(1)
	v_mfma_f32_16x16x128_f8f6f4 v[62:65], v[18:25], v[210:217], 0
	v_mfma_f32_16x16x128_f8f6f4 v[58:61], v[26:33], v[210:217], 0
	s_waitcnt lgkmcnt(0)
	v_mfma_f32_16x16x128_f8f6f4 v[46:49], v[18:25], v[218:225], 0
	v_mfma_f32_16x16x128_f8f6f4 v[42:45], v[26:33], v[218:225], 0
	s_setprio 0
	s_setprio 1
	v_mfma_f32_16x16x128_f8f6f4 v[86:89], v[2:9], v[194:201], 0
	v_mfma_f32_16x16x128_f8f6f4 v[82:85], v[10:17], v[194:201], 0
	v_mfma_f32_16x16x128_f8f6f4 v[70:73], v[2:9], v[202:209], 0
	v_mfma_f32_16x16x128_f8f6f4 v[66:69], v[10:17], v[202:209], 0
	v_mfma_f32_16x16x128_f8f6f4 v[54:57], v[2:9], v[210:217], 0
	v_mfma_f32_16x16x128_f8f6f4 v[50:53], v[10:17], v[210:217], 0
	v_mfma_f32_16x16x128_f8f6f4 v[38:41], v[2:9], v[218:225], 0
	v_mfma_f32_16x16x128_f8f6f4 v[34:37], v[10:17], v[218:225], 0
	s_setprio 0
	s_barrier
	s_add_i32 s68, 0, 0x18000
	v_add_u32_e32 v183, s68, v174
	v_add_u32_e32 v184, s68, v175
	s_add_i32 s68, 0, 0x1c000
	v_add_u32_e32 v185, s68, v174
	ds_read_b128 v[2:5], v183
	ds_read_b128 v[10:13], v183 offset:2048
	ds_read_b128 v[6:9], v184
	ds_read_b128 v[14:17], v184 offset:2048
	v_add_u32_e32 v186, s68, v175
	ds_read_b128 v[18:21], v185
	ds_read_b128 v[26:29], v185 offset:2048
	ds_read_b128 v[22:25], v186
	ds_read_b128 v[30:33], v186 offset:2048
	ds_read_b128 v[194:197], v180 offset:32768
	ds_read_b128 v[202:205], v180 offset:34816
	ds_read_b128 v[198:201], v181 offset:32768
	ds_read_b128 v[206:209], v181 offset:34816
	ds_read_b128 v[210:213], v180 offset:36864
	ds_read_b128 v[218:221], v180 offset:38912
	ds_read_b128 v[214:217], v181 offset:36864
	ds_read_b128 v[222:225], v181 offset:38912
	s_mov_b32 m0, s50
	s_nop 0
	global_load_lds_dwordx4 v163, s[46:47] offset:0
	s_nop 0
	s_mov_b32 m0, s51
	s_nop 0
	global_load_lds_dwordx4 v171, s[46:47] offset:0
	s_waitcnt vmcnt(8)
	s_waitcnt lgkmcnt(0)
	s_barrier
	s_setprio 1
	s_waitcnt lgkmcnt(5)
	v_mfma_f32_16x16x128_f8f6f4 v[158:161], v[2:9], v[194:201], v[158:161]
	v_mfma_f32_16x16x128_f8f6f4 v[154:157], v[10:17], v[194:201], v[154:157]
	s_waitcnt lgkmcnt(4)
	v_mfma_f32_16x16x128_f8f6f4 v[142:145], v[2:9], v[202:209], v[142:145]
	v_mfma_f32_16x16x128_f8f6f4 v[138:141], v[10:17], v[202:209], v[138:141]
	s_waitcnt lgkmcnt(1)
	v_mfma_f32_16x16x128_f8f6f4 v[126:129], v[2:9], v[210:217], v[126:129]
	v_mfma_f32_16x16x128_f8f6f4 v[122:125], v[10:17], v[210:217], v[122:125]
	s_waitcnt lgkmcnt(0)
	v_mfma_f32_16x16x128_f8f6f4 v[110:113], v[2:9], v[218:225], v[110:113]
	v_mfma_f32_16x16x128_f8f6f4 v[106:109], v[10:17], v[218:225], v[106:109]
	s_setprio 0
	s_setprio 1
	v_mfma_f32_16x16x128_f8f6f4 v[150:153], v[18:25], v[194:201], v[150:153]
	v_mfma_f32_16x16x128_f8f6f4 v[146:149], v[26:33], v[194:201], v[146:149]
	v_mfma_f32_16x16x128_f8f6f4 v[134:137], v[18:25], v[202:209], v[134:137]
	v_mfma_f32_16x16x128_f8f6f4 v[130:133], v[26:33], v[202:209], v[130:133]
	v_mfma_f32_16x16x128_f8f6f4 v[118:121], v[18:25], v[210:217], v[118:121]
	v_mfma_f32_16x16x128_f8f6f4 v[114:117], v[26:33], v[210:217], v[114:117]
	v_mfma_f32_16x16x128_f8f6f4 v[102:105], v[18:25], v[218:225], v[102:105]
	v_mfma_f32_16x16x128_f8f6f4 v[98:101], v[26:33], v[218:225], v[98:101]
	s_setprio 0
	s_barrier
	ds_read_b128 v[194:197], v180 offset:49152
	ds_read_b128 v[202:205], v180 offset:51200
	ds_read_b128 v[198:201], v181 offset:49152
	ds_read_b128 v[206:209], v181 offset:51200
	ds_read_b128 v[210:213], v180 offset:53248
	ds_read_b128 v[218:221], v180 offset:55296
	ds_read_b128 v[214:217], v181 offset:53248
	ds_read_b128 v[222:225], v181 offset:55296
	s_add_u32 s46, s66, 0x180
	s_addc_u32 s47, s67, 0
	s_mov_b32 m0, s52
	s_nop 0
	global_load_lds_dwordx4 v172, s[46:47] offset:0
	s_nop 0
	s_mov_b32 m0, s53
	s_nop 0
	global_load_lds_dwordx4 v173, s[46:47] offset:0
	s_add_u32 s46, s66, 0x20180
	s_addc_u32 s47, s67, 0
	s_mov_b32 m0, s56
	s_nop 0
	global_load_lds_dwordx4 v172, s[46:47] offset:0
	s_nop 0
	s_mov_b32 m0, s57
	s_nop 0
	global_load_lds_dwordx4 v173, s[46:47] offset:0
	s_add_u32 s46, s64, 0x180
	s_addc_u32 s47, s65, 0
	s_mov_b32 m0, s54
	s_nop 0
	global_load_lds_dwordx4 v162, s[46:47] offset:0
	s_nop 0
	s_mov_b32 m0, s55
	s_nop 0
	global_load_lds_dwordx4 v170, s[46:47] offset:0
	s_waitcnt vmcnt(8)
	s_waitcnt lgkmcnt(0)
	s_barrier
	s_setprio 1
	s_waitcnt lgkmcnt(5)
	v_mfma_f32_16x16x128_f8f6f4 v[94:97], v[2:9], v[194:201], v[94:97]
	v_mfma_f32_16x16x128_f8f6f4 v[90:93], v[10:17], v[194:201], v[90:93]
	s_waitcnt lgkmcnt(4)
	v_mfma_f32_16x16x128_f8f6f4 v[78:81], v[2:9], v[202:209], v[78:81]
	v_mfma_f32_16x16x128_f8f6f4 v[74:77], v[10:17], v[202:209], v[74:77]
	s_waitcnt lgkmcnt(1)
	v_mfma_f32_16x16x128_f8f6f4 v[62:65], v[2:9], v[210:217], v[62:65]
	v_mfma_f32_16x16x128_f8f6f4 v[58:61], v[10:17], v[210:217], v[58:61]
	s_waitcnt lgkmcnt(0)
	v_mfma_f32_16x16x128_f8f6f4 v[46:49], v[2:9], v[218:225], v[46:49]
	v_mfma_f32_16x16x128_f8f6f4 v[42:45], v[10:17], v[218:225], v[42:45]
	s_setprio 0
	s_setprio 1
	v_mfma_f32_16x16x128_f8f6f4 v[86:89], v[18:25], v[194:201], v[86:89]
	v_mfma_f32_16x16x128_f8f6f4 v[82:85], v[26:33], v[194:201], v[82:85]
	v_mfma_f32_16x16x128_f8f6f4 v[70:73], v[18:25], v[202:209], v[70:73]
	v_mfma_f32_16x16x128_f8f6f4 v[66:69], v[26:33], v[202:209], v[66:69]
	v_mfma_f32_16x16x128_f8f6f4 v[54:57], v[18:25], v[210:217], v[54:57]
	v_mfma_f32_16x16x128_f8f6f4 v[50:53], v[26:33], v[210:217], v[50:53]
	v_mfma_f32_16x16x128_f8f6f4 v[38:41], v[18:25], v[218:225], v[38:41]
	v_mfma_f32_16x16x128_f8f6f4 v[34:37], v[26:33], v[218:225], v[34:37]
	s_setprio 0
	s_barrier
	s_add_i32 s35, s35, 2
	s_add_u32 s4, s4, 0x100
	s_addc_u32 s5, s5, 0
